# P23: only the leading wave half (waves 0-3) carries epilogue VALU in its last K-iteration; the lagging half runs its whole epilogue after the loop (no VALU contention between SIMD partners)
# speedup vs baseline: 1.0054x; 1.0028x over previous
.Ltx23_skip:
	ds_read_b128 v[2:5], v184
	ds_read_b128 v[6:9], v185
	ds_read_b128 v[10:13], v192
	ds_read_b128 v[14:17], v193
	ds_read_b128 v[18:21], v186
	ds_read_b128 v[22:25], v187
	ds_read_b128 v[26:29], v194
	ds_read_b128 v[30:33], v195
	v_mov_b32_e32 v172, v176
	ds_read_b128 v[164:167], v196 offset:32768
	ds_read_b128 v[168:171], v196 offset:33792
	ds_read_b128 v[198:201], v196 offset:34816
	ds_read_b128 v[202:205], v196 offset:35840
	ds_read_b128 v[214:217], v196 offset:36864
	ds_read_b128 v[218:221], v196 offset:37888
	ds_read_b128 v[222:225], v196 offset:38912
	ds_read_b128 v[226:229], v196 offset:39936
	s_add_i32 s86, s86, s47
	s_mov_b32 m0, s55
	v_add_u32_e32 v172, s86, v172
	global_load_lds_dwordx4 v172, s[4:5]
	v_mov_b32_e32 v172, v176
	s_add_i32 s86, s86, s47
	v_add_u32_e32 v172, s86, v172
	s_mov_b32 m0, s56
	s_nop 0
	global_load_lds_dwordx4 v172, s[4:5]
	s_waitcnt vmcnt(8)
	s_waitcnt lgkmcnt(0)
	s_barrier
	s_setprio 1
	s_waitcnt lgkmcnt(0)
	v_mfma_f32_16x16x128_f8f6f4 v[158:161], v[2:9], v[164:171], v[158:161]
	v_mfma_f32_16x16x128_f8f6f4 v[154:157], v[10:17], v[164:171], v[154:157]
	v_mfma_f32_16x16x128_f8f6f4 v[150:153], v[2:9], v[198:205], v[150:153]
	v_mfma_f32_16x16x128_f8f6f4 v[146:149], v[10:17], v[198:205], v[146:149]
	v_mfma_f32_16x16x128_f8f6f4 v[138:141], v[2:9], v[214:221], v[138:141]
	v_mfma_f32_16x16x128_f8f6f4 v[130:133], v[10:17], v[214:221], v[130:133]
	v_mfma_f32_16x16x128_f8f6f4 v[122:125], v[2:9], v[222:229], v[122:125]
	v_mfma_f32_16x16x128_f8f6f4 v[114:117], v[10:17], v[222:229], v[114:117]
	s_setprio 0
	s_setprio 1
	v_mfma_f32_16x16x128_f8f6f4 v[142:145], v[18:25], v[164:171], v[142:145]
	v_mfma_f32_16x16x128_f8f6f4 v[134:137], v[26:33], v[164:171], v[134:137]
	v_mfma_f32_16x16x128_f8f6f4 v[126:129], v[18:25], v[198:205], v[126:129]
	v_mfma_f32_16x16x128_f8f6f4 v[118:121], v[26:33], v[198:205], v[118:121]
	v_mfma_f32_16x16x128_f8f6f4 v[110:113], v[18:25], v[214:221], v[110:113]
	v_mfma_f32_16x16x128_f8f6f4 v[106:109], v[26:33], v[214:221], v[106:109]
	v_mfma_f32_16x16x128_f8f6f4 v[102:105], v[18:25], v[222:229], v[102:105]
	v_mfma_f32_16x16x128_f8f6f4 v[98:101], v[26:33], v[222:229], v[98:101]
	s_setprio 0
	s_barrier
	s_cmp_eq_u32 s67, s83
	s_cbranch_scc0 .Lh23_nolast
	s_cmp_lg_u64 s[16:17], 0
	s_cbranch_scc1 .Lh23_last
.Lh23_nolast:
	v_mov_b32_e32 v172, v177
	ds_read_b128 v[164:167], v196 offset:49152
	ds_read_b128 v[168:171], v196 offset:50176
	ds_read_b128 v[198:201], v196 offset:51200
	ds_read_b128 v[202:205], v196 offset:52224
	ds_read_b128 v[214:217], v196 offset:53248
	ds_read_b128 v[218:221], v196 offset:54272
	ds_read_b128 v[222:225], v196 offset:55296
	ds_read_b128 v[226:229], v196 offset:56320
	s_mov_b32 m0, s58
	v_add_u32_e32 v172, s85, v172
	global_load_lds_dwordx4 v172, s[6:7]
	v_mov_b32_e32 v172, v177
	s_add_i32 s85, s85, s48
	v_add_u32_e32 v172, s85, v172
	s_mov_b32 m0, s59
	s_add_i32 s85, s85, s48
	global_load_lds_dwordx4 v172, s[6:7]
	v_mov_b32_e32 v172, v177
	s_mov_b32 m0, s62
	v_add_u32_e32 v172, s85, v172
	global_load_lds_dwordx4 v172, s[6:7]
	v_mov_b32_e32 v172, v177
	s_add_i32 s85, s85, s48
	v_add_u32_e32 v172, s85, v172
	s_mov_b32 m0, s63
	s_nop 0
	global_load_lds_dwordx4 v172, s[6:7]
	v_mov_b32_e32 v172, v176
	s_mov_b32 m0, s60
	v_add_u32_e32 v172, s84, v172
	global_load_lds_dwordx4 v172, s[4:5]
	v_mov_b32_e32 v172, v176
	s_add_i32 s84, s84, s47
	v_add_u32_e32 v172, s84, v172
	s_mov_b32 m0, s61
	s_nop 0
	global_load_lds_dwordx4 v172, s[4:5]
	s_waitcnt vmcnt(8)
	s_waitcnt lgkmcnt(0)
	s_barrier
	s_setprio 1
	s_waitcnt lgkmcnt(0)
	v_mfma_f32_16x16x128_f8f6f4 v[94:97], v[2:9], v[164:171], v[94:97]
	v_mfma_f32_16x16x128_f8f6f4 v[90:93], v[10:17], v[164:171], v[90:93]
	v_mfma_f32_16x16x128_f8f6f4 v[86:89], v[2:9], v[198:205], v[86:89]
	v_mfma_f32_16x16x128_f8f6f4 v[82:85], v[10:17], v[198:205], v[82:85]
	v_mfma_f32_16x16x128_f8f6f4 v[74:77], v[2:9], v[214:221], v[74:77]
	v_mfma_f32_16x16x128_f8f6f4 v[66:69], v[10:17], v[214:221], v[66:69]
	v_mfma_f32_16x16x128_f8f6f4 v[58:61], v[2:9], v[222:229], v[58:61]
	v_mfma_f32_16x16x128_f8f6f4 v[50:53], v[10:17], v[222:229], v[50:53]
	s_setprio 0
	s_setprio 1
	v_mfma_f32_16x16x128_f8f6f4 v[78:81], v[18:25], v[164:171], v[78:81]
	v_mfma_f32_16x16x128_f8f6f4 v[70:73], v[26:33], v[164:171], v[70:73]
	v_mfma_f32_16x16x128_f8f6f4 v[62:65], v[18:25], v[198:205], v[62:65]
	v_mfma_f32_16x16x128_f8f6f4 v[54:57], v[26:33], v[198:205], v[54:57]
	v_mfma_f32_16x16x128_f8f6f4 v[46:49], v[18:25], v[214:221], v[46:49]
	v_mfma_f32_16x16x128_f8f6f4 v[42:45], v[26:33], v[214:221], v[42:45]
	v_mfma_f32_16x16x128_f8f6f4 v[38:41], v[18:25], v[222:229], v[38:41]
	v_mfma_f32_16x16x128_f8f6f4 v[34:37], v[26:33], v[222:229], v[34:37]
	s_setprio 0
	s_barrier
	s_add_i32 s83, s83, 2
	s_addk_i32 s28, 0x100
	s_addk_i32 s82, 0x100
	s_cmp_ge_i32 s83, s64
	s_cbranch_scc0 .LBB0_2937
	s_branch .LBB0_2939
